# v12 plus nt on the P1 bf16 h stores (consumed only by the late bf16 in-projection units)
# baseline (speedup 1.0000x reference)
.LBB0_120:
	s_andn2_b64 vcc, exec, s[44:45]
	s_cbranch_vccnz .LBB0_122
	v_lshlrev_b32_e32 v167, 1, v184
	v_cvt_pk_bf16_f32 v168, v162, v163
	v_cvt_pk_bf16_f32 v169, v164, v165
	global_store_dwordx2 v167, v[168:169], s[0:1] nt

.LBB0_124:
	s_andn2_b64 vcc, exec, s[42:43]
	s_cbranch_vccnz .LBB0_126
	v_lshlrev_b32_e32 v174, 1, v184
	v_cvt_pk_bf16_f32 v172, v162, v163
	v_cvt_pk_bf16_f32 v173, v164, v165
	global_store_dwordx2 v174, v[172:173], s[0:1] offset:512 nt

.LBB0_128:
	s_andn2_b64 vcc, exec, s[42:43]
	s_cbranch_vccnz .LBB0_130
	v_lshlrev_b32_e32 v174, 1, v184
	v_cvt_pk_bf16_f32 v172, v162, v163
	v_cvt_pk_bf16_f32 v173, v164, v165
	global_store_dwordx2 v174, v[172:173], s[0:1] offset:1024 nt

.LBB0_132:
	s_andn2_b64 vcc, exec, s[42:43]
	s_cbranch_vccnz .LBB0_134
	v_lshlrev_b32_e32 v172, 1, v184
	v_cvt_pk_bf16_f32 v170, v162, v163
	v_cvt_pk_bf16_f32 v171, v164, v165
	global_store_dwordx2 v172, v[170:171], s[0:1] offset:1536 nt

.LBB0_136:
	s_andn2_b64 vcc, exec, s[42:43]
	s_cbranch_vccnz .LBB0_138
	v_lshlrev_b32_e32 v171, 1, v184
	v_cvt_pk_bf16_f32 v172, v162, v163
	v_cvt_pk_bf16_f32 v173, v164, v165
	global_store_dwordx2 v171, v[172:173], s[0:1] offset:2048 nt

.LBB0_140:
	s_andn2_b64 vcc, exec, s[42:43]
	s_cbranch_vccnz .LBB0_142
	v_lshlrev_b32_e32 v174, 1, v184
	v_cvt_pk_bf16_f32 v172, v162, v163
	v_cvt_pk_bf16_f32 v173, v164, v165
	global_store_dwordx2 v174, v[172:173], s[0:1] offset:2560 nt

.LBB0_144:
	s_andn2_b64 vcc, exec, s[42:43]
	s_cbranch_vccnz .LBB0_146
	v_lshlrev_b32_e32 v173, 1, v184
	v_cvt_pk_bf16_f32 v174, v162, v163
	v_cvt_pk_bf16_f32 v175, v164, v165
	global_store_dwordx2 v173, v[174:175], s[0:1] offset:3072 nt

.LBB0_148:
	s_andn2_b64 vcc, exec, s[12:13]
	s_cbranch_vccnz .LBB0_150
	v_lshlrev_b32_e32 v174, 1, v184
	v_cvt_pk_bf16_f32 v166, v162, v163
	v_cvt_pk_bf16_f32 v167, v164, v165
	global_store_dwordx2 v174, v[166:167], s[0:1] offset:3584 nt
